# baseline (speedup 1.0000x reference)
.LBB1_2:
	s_mul_i32 s41, s34, 0x30000
	s_mul_hi_i32 s40, s34, 0x30000
	s_add_u32 s11, s6, s41
	s_addc_u32 s35, s7, s40
	s_mov_b32 s10, s2
	s_add_u32 s2, s11, 0x6000
	s_addc_u32 s3, s35, 0
	s_mul_i32 s43, s13, 0x30000
	s_mul_hi_i32 s42, s13, 0x30000
	s_add_u32 s44, s4, s43
	s_addc_u32 s45, s5, s42
	s_add_u32 s38, s11, 0x8000
	s_addc_u32 s39, s35, 0
	s_add_u32 s46, s44, 0x5000
	s_addc_u32 s47, s45, 0
	s_and_b64 s[36:37], s[0:1], exec
	s_cselect_b32 s37, s39, s47
	s_cselect_b32 s36, s38, s46
	s_add_u32 s38, s44, 0x7000
	s_addc_u32 s39, s45, 0
	s_add_u32 s2, s11, 0x9000
	s_addc_u32 s3, s35, 0
	s_add_u32 s11, s11, 0xb000
	s_addc_u32 s35, s35, 0
	s_add_u32 s38, s44, 0x8000
	s_addc_u32 s39, s45, 0
	s_and_b64 s[36:37], s[0:1], exec
	s_cselect_b32 s37, s35, s39
	s_cselect_b32 s36, s11, s38
	s_add_u32 s38, s44, 0xa000
	s_addc_u32 s39, s45, 0
	s_add_u32 s11, s21, s43
	s_addc_u32 s35, s22, s42
	s_add_u32 s2, s23, s41
	s_addc_u32 s3, s24, s40
	s_cmp_eq_u32 s74, 1
	s_cselect_b32 s72, s11, s2
	s_cselect_b32 s73, s35, s3
	s_add_u32 s72, s72, s75
	s_addc_u32 s73, s73, 0
	s_cmp_eq_u32 s66, 0
	s_cselect_b64 vcc, exec, 0
	s_waitcnt lgkmcnt(0)

.Lpst3_join:
	v_mfma_scale_f32_16x16x128_f8f6f4 v[80:83], v[46:51], v[40:45], v[80:83], v187, v187 op_sel_hi:[0,0,0] cbsz:2 blgp:2
	v_mfma_scale_f32_16x16x128_f8f6f4 v[72:75], v[194:199], v[40:45], v[72:75], v187, v187 op_sel_hi:[0,0,0] cbsz:2 blgp:2
	v_mfma_scale_f32_16x16x128_f8f6f4 v[64:67], v[200:205], v[40:45], v[64:67], v187, v187 op_sel_hi:[0,0,0] cbsz:2 blgp:2
	v_mfma_scale_f32_16x16x128_f8f6f4 v[56:59], v[206:211], v[40:45], v[56:59], v187, v187 op_sel_hi:[0,0,0] cbsz:2 blgp:2
	v_mfma_scale_f32_16x16x128_f8f6f4 v[52:55], v[46:51], v[188:193], v[52:55], v187, v187 op_sel_hi:[0,0,0] cbsz:2 blgp:2
	v_mfma_scale_f32_16x16x128_f8f6f4 v[48:51], v[194:199], v[188:193], v[224:227], v187, v187 op_sel_hi:[0,0,0] cbsz:2 blgp:2
	v_mfma_scale_f32_16x16x128_f8f6f4 v[44:47], v[200:205], v[188:193], v[212:215], v187, v187 op_sel_hi:[0,0,0] cbsz:2 blgp:2
	v_mfma_scale_f32_16x16x128_f8f6f4 v[40:43], v[206:211], v[188:193], v[216:219], v187, v187 op_sel_hi:[0,0,0] cbsz:2 blgp:2
	s_add_u32 s11, s11, 0xc000
	s_addc_u32 s35, s35, 0
	s_add_u32 s2, s2, 0xc000
	s_addc_u32 s3, s3, 0
	s_add_u32 s72, s72, 0xc000
	s_addc_u32 s73, s73, 0
	s_waitcnt lgkmcnt(0)
	ds_read_b128 v[188:191], v1 offset:24576
	ds_read_b64 v[192:193], v172 offset:24640
	ds_read_b128 v[194:197], v1 offset:26112
	ds_read_b64 v[198:199], v172 offset:26176
	ds_read_b128 v[200:203], v170 offset:36864
	ds_read_b64 v[204:205], v173 offset:36928
	ds_read_b128 v[206:209], v170 offset:38400
	ds_read_b64 v[210:211], v173 offset:38464
	ds_read_b128 v[212:215], v170 offset:39936
	ds_read_b64 v[216:217], v173 offset:40000
	ds_read_b128 v[218:221], v170 offset:41472
	ds_read_b64 v[222:223], v173 offset:41536
	v_mfma_scale_f32_16x16x128_f8f6f4 v[164:167], v[2:7], v[20:25], v[164:167], v187, v187 op_sel_hi:[0,0,0] cbsz:2 blgp:2
	v_mfma_scale_f32_16x16x128_f8f6f4 v[160:163], v[8:13], v[20:25], v[160:163], v187, v187 op_sel_hi:[0,0,0] cbsz:2 blgp:2
	v_mfma_scale_f32_16x16x128_f8f6f4 v[156:159], v[14:19], v[20:25], v[156:159], v187, v187 op_sel_hi:[0,0,0] cbsz:2 blgp:2
	v_mfma_scale_f32_16x16x128_f8f6f4 v[152:155], v[26:31], v[20:25], v[152:155], v187, v187 op_sel_hi:[0,0,0] cbsz:2 blgp:2
	v_mfma_scale_f32_16x16x128_f8f6f4 v[148:151], v[2:7], v[32:37], v[148:151], v187, v187 op_sel_hi:[0,0,0] cbsz:2 blgp:2
	v_mfma_scale_f32_16x16x128_f8f6f4 v[140:143], v[8:13], v[32:37], v[140:143], v187, v187 op_sel_hi:[0,0,0] cbsz:2 blgp:2
	v_mfma_scale_f32_16x16x128_f8f6f4 v[132:135], v[14:19], v[32:37], v[132:135], v187, v187 op_sel_hi:[0,0,0] cbsz:2 blgp:2
	v_mfma_scale_f32_16x16x128_f8f6f4 v[124:127], v[26:31], v[32:37], v[124:127], v187, v187 op_sel_hi:[0,0,0] cbsz:2 blgp:2
	s_cbranch_vccz .Lua0_other
	s_add_u32 s38, s72, 0xffffa000
	s_addc_u32 s39, s73, -1
	s_waitcnt vmcnt(0)
	s_barrier
	s_mov_b32 m0, s76
	s_nop 0
	global_load_lds_dwordx4 v228, s[38:39] offset:-3072
	global_load_lds_dwordx4 v228, s[38:39] offset:-2048
	global_load_lds_dwordx4 v228, s[38:39] offset:-1024
	global_load_lds_dwordx4 v228, s[38:39]
	global_load_lds_dwordx4 v228, s[38:39] offset:1024
	global_load_lds_dwordx4 v228, s[38:39] offset:2048
	s_branch .Lua0_join

.Lub3_join:
	v_mfma_scale_f32_16x16x128_f8f6f4 v[80:83], v[46:51], v[40:45], v[80:83], v187, v187 op_sel_hi:[0,0,0] cbsz:2 blgp:2
	v_mfma_scale_f32_16x16x128_f8f6f4 v[72:75], v[194:199], v[40:45], v[72:75], v187, v187 op_sel_hi:[0,0,0] cbsz:2 blgp:2
	v_mfma_scale_f32_16x16x128_f8f6f4 v[64:67], v[200:205], v[40:45], v[64:67], v187, v187 op_sel_hi:[0,0,0] cbsz:2 blgp:2
	v_mfma_scale_f32_16x16x128_f8f6f4 v[56:59], v[206:211], v[40:45], v[56:59], v187, v187 op_sel_hi:[0,0,0] cbsz:2 blgp:2
	v_mfma_scale_f32_16x16x128_f8f6f4 v[52:55], v[46:51], v[188:193], v[52:55], v187, v187 op_sel_hi:[0,0,0] cbsz:2 blgp:2
	v_mfma_scale_f32_16x16x128_f8f6f4 v[48:51], v[194:199], v[188:193], v[224:227], v187, v187 op_sel_hi:[0,0,0] cbsz:2 blgp:2
	v_mfma_scale_f32_16x16x128_f8f6f4 v[44:47], v[200:205], v[188:193], v[212:215], v187, v187 op_sel_hi:[0,0,0] cbsz:2 blgp:2
	v_mfma_scale_f32_16x16x128_f8f6f4 v[40:43], v[206:211], v[188:193], v[216:219], v187, v187 op_sel_hi:[0,0,0] cbsz:2 blgp:2
	s_waitcnt lgkmcnt(0)

.Ltail_nowait:
	s_barrier
	s_waitcnt lgkmcnt(0)
	v_mfma_scale_f32_16x16x128_f8f6f4 v[112:115], v[2:7], v[188:193], v[112:115], v187, v187 op_sel_hi:[0,0,0] cbsz:2 blgp:2
	v_mfma_scale_f32_16x16x128_f8f6f4 v[100:103], v[8:13], v[188:193], v[100:103], v187, v187 op_sel_hi:[0,0,0] cbsz:2 blgp:2
	v_mfma_scale_f32_16x16x128_f8f6f4 v[92:95], v[14:19], v[188:193], v[92:95], v187, v187 op_sel_hi:[0,0,0] cbsz:2 blgp:2
	v_mfma_scale_f32_16x16x128_f8f6f4 v[88:91], v[26:31], v[188:193], v[88:91], v187, v187 op_sel_hi:[0,0,0] cbsz:2 blgp:2
	v_mfma_scale_f32_16x16x128_f8f6f4 v[84:87], v[2:7], v[194:199], v[84:87], v187, v187 op_sel_hi:[0,0,0] cbsz:2 blgp:2
	v_mfma_scale_f32_16x16x128_f8f6f4 v[76:79], v[8:13], v[194:199], v[76:79], v187, v187 op_sel_hi:[0,0,0] cbsz:2 blgp:2
	v_mfma_scale_f32_16x16x128_f8f6f4 v[68:71], v[14:19], v[194:199], v[68:71], v187, v187 op_sel_hi:[0,0,0] cbsz:2 blgp:2
	v_mfma_scale_f32_16x16x128_f8f6f4 v[60:63], v[26:31], v[194:199], v[60:63], v187, v187 op_sel_hi:[0,0,0] cbsz:2 blgp:2
	ds_read_b128 v[2:5], v170 offset:61440
	ds_read_b64 v[6:7], v173 offset:61504
	ds_read_b128 v[8:11], v170 offset:62976
	ds_read_b64 v[12:13], v173 offset:63040
	ds_read_b128 v[14:17], v170 offset:64512
	ds_read_b64 v[18:19], v173 offset:64576
	ds_read_b128 v[26:29], v171 offset:53760
	ds_read_b64 v[30:31], v174 offset:53760
	v_mfma_scale_f32_16x16x128_f8f6f4 v[144:147], v[200:205], v[20:25], v[144:147], v187, v187 op_sel_hi:[0,0,0] cbsz:2 blgp:2
	v_mfma_scale_f32_16x16x128_f8f6f4 v[136:139], v[206:211], v[20:25], v[136:139], v187, v187 op_sel_hi:[0,0,0] cbsz:2 blgp:2
	v_mfma_scale_f32_16x16x128_f8f6f4 v[128:131], v[212:217], v[20:25], v[128:131], v187, v187 op_sel_hi:[0,0,0] cbsz:2 blgp:2
	v_mfma_scale_f32_16x16x128_f8f6f4 v[120:123], v[218:223], v[20:25], v[120:123], v187, v187 op_sel_hi:[0,0,0] cbsz:2 blgp:2
	v_mfma_scale_f32_16x16x128_f8f6f4 v[116:119], v[200:205], v[32:37], v[116:119], v187, v187 op_sel_hi:[0,0,0] cbsz:2 blgp:2
	v_mfma_scale_f32_16x16x128_f8f6f4 v[108:111], v[206:211], v[32:37], v[108:111], v187, v187 op_sel_hi:[0,0,0] cbsz:2 blgp:2
	v_mfma_scale_f32_16x16x128_f8f6f4 v[104:107], v[212:217], v[32:37], v[104:107], v187, v187 op_sel_hi:[0,0,0] cbsz:2 blgp:2
	v_mfma_scale_f32_16x16x128_f8f6f4 v[96:99], v[218:223], v[32:37], v[96:99], v187, v187 op_sel_hi:[0,0,0] cbsz:2 blgp:2
	ds_read_b128 v[20:23], v1 offset:49152
	ds_read_b64 v[24:25], v172 offset:49216
	ds_read_b128 v[32:35], v1 offset:50688
	ds_read_b64 v[36:37], v172 offset:50752
	s_waitcnt vmcnt(0)
	s_barrier
	v_mfma_scale_f32_16x16x128_f8f6f4 v[80:83], v[200:205], v[188:193], v[80:83], v187, v187 op_sel_hi:[0,0,0] cbsz:2 blgp:2
	v_mfma_scale_f32_16x16x128_f8f6f4 v[72:75], v[206:211], v[188:193], v[72:75], v187, v187 op_sel_hi:[0,0,0] cbsz:2 blgp:2
	v_mfma_scale_f32_16x16x128_f8f6f4 v[64:67], v[212:217], v[188:193], v[64:67], v187, v187 op_sel_hi:[0,0,0] cbsz:2 blgp:2
	v_mfma_scale_f32_16x16x128_f8f6f4 v[56:59], v[218:223], v[188:193], v[56:59], v187, v187 op_sel_hi:[0,0,0] cbsz:2 blgp:2
	v_mfma_scale_f32_16x16x128_f8f6f4 v[52:55], v[200:205], v[194:199], v[52:55], v187, v187 op_sel_hi:[0,0,0] cbsz:2 blgp:2
	v_mfma_scale_f32_16x16x128_f8f6f4 v[224:227], v[206:211], v[194:199], v[48:51], v187, v187 op_sel_hi:[0,0,0] cbsz:2 blgp:2
	v_mfma_scale_f32_16x16x128_f8f6f4 v[212:215], v[212:217], v[194:199], v[44:47], v187, v187 op_sel_hi:[0,0,0] cbsz:2 blgp:2
	v_mfma_scale_f32_16x16x128_f8f6f4 v[216:219], v[218:223], v[194:199], v[40:43], v187, v187 op_sel_hi:[0,0,0] cbsz:2 blgp:2
	s_waitcnt lgkmcnt(0)
	s_nop 0
	ds_read_b128 v[40:43], v175
	ds_read_b64 v[44:45], v176
	ds_read_b128 v[188:191], v179
	ds_read_b64 v[192:193], v180
	ds_read_b128 v[46:49], v177
	ds_read_b64 v[50:51], v178
	ds_read_b128 v[194:197], v181
	ds_read_b64 v[198:199], v182
	ds_read_b128 v[200:203], v183
	ds_read_b64 v[204:205], v184
	ds_read_b128 v[206:209], v185
	ds_read_b64 v[210:211], v186
	v_mfma_scale_f32_16x16x128_f8f6f4 v[164:167], v[2:7], v[20:25], v[164:167], v187, v187 op_sel_hi:[0,0,0] cbsz:2 blgp:2
	v_mfma_scale_f32_16x16x128_f8f6f4 v[160:163], v[8:13], v[20:25], v[160:163], v187, v187 op_sel_hi:[0,0,0] cbsz:2 blgp:2
	v_mfma_scale_f32_16x16x128_f8f6f4 v[156:159], v[14:19], v[20:25], v[156:159], v187, v187 op_sel_hi:[0,0,0] cbsz:2 blgp:2
	v_mfma_scale_f32_16x16x128_f8f6f4 v[152:155], v[26:31], v[20:25], v[152:155], v187, v187 op_sel_hi:[0,0,0] cbsz:2 blgp:2
	v_mfma_scale_f32_16x16x128_f8f6f4 v[148:151], v[2:7], v[32:37], v[148:151], v187, v187 op_sel_hi:[0,0,0] cbsz:2 blgp:2
	v_mfma_scale_f32_16x16x128_f8f6f4 v[140:143], v[8:13], v[32:37], v[140:143], v187, v187 op_sel_hi:[0,0,0] cbsz:2 blgp:2
	v_mfma_scale_f32_16x16x128_f8f6f4 v[132:135], v[14:19], v[32:37], v[132:135], v187, v187 op_sel_hi:[0,0,0] cbsz:2 blgp:2
	v_mfma_scale_f32_16x16x128_f8f6f4 v[124:127], v[26:31], v[32:37], v[124:127], v187, v187 op_sel_hi:[0,0,0] cbsz:2 blgp:2
	s_waitcnt lgkmcnt(0)
	v_mfma_scale_f32_16x16x128_f8f6f4 v[112:115], v[2:7], v[40:45], v[112:115], v187, v187 op_sel_hi:[0,0,0] cbsz:2 blgp:2
	v_mfma_scale_f32_16x16x128_f8f6f4 v[100:103], v[8:13], v[40:45], v[100:103], v187, v187 op_sel_hi:[0,0,0] cbsz:2 blgp:2
	v_mfma_scale_f32_16x16x128_f8f6f4 v[92:95], v[14:19], v[40:45], v[92:95], v187, v187 op_sel_hi:[0,0,0] cbsz:2 blgp:2
	v_mfma_scale_f32_16x16x128_f8f6f4 v[88:91], v[26:31], v[40:45], v[88:91], v187, v187 op_sel_hi:[0,0,0] cbsz:2 blgp:2
	v_mfma_scale_f32_16x16x128_f8f6f4 v[84:87], v[2:7], v[188:193], v[84:87], v187, v187 op_sel_hi:[0,0,0] cbsz:2 blgp:2
	v_mfma_scale_f32_16x16x128_f8f6f4 v[76:79], v[8:13], v[188:193], v[76:79], v187, v187 op_sel_hi:[0,0,0] cbsz:2 blgp:2
	v_mfma_scale_f32_16x16x128_f8f6f4 v[68:71], v[14:19], v[188:193], v[68:71], v187, v187 op_sel_hi:[0,0,0] cbsz:2 blgp:2
	v_mfma_scale_f32_16x16x128_f8f6f4 v[60:63], v[26:31], v[188:193], v[60:63], v187, v187 op_sel_hi:[0,0,0] cbsz:2 blgp:2
	v_mfma_scale_f32_16x16x128_f8f6f4 v[144:147], v[46:51], v[20:25], v[144:147], v187, v187 op_sel_hi:[0,0,0] cbsz:2 blgp:2
	v_mfma_scale_f32_16x16x128_f8f6f4 v[136:139], v[194:199], v[20:25], v[136:139], v187, v187 op_sel_hi:[0,0,0] cbsz:2 blgp:2
	v_mfma_scale_f32_16x16x128_f8f6f4 v[128:131], v[200:205], v[20:25], v[128:131], v187, v187 op_sel_hi:[0,0,0] cbsz:2 blgp:2
	v_mfma_scale_f32_16x16x128_f8f6f4 v[120:123], v[206:211], v[20:25], v[120:123], v187, v187 op_sel_hi:[0,0,0] cbsz:2 blgp:2
	v_mfma_scale_f32_16x16x128_f8f6f4 v[116:119], v[46:51], v[32:37], v[116:119], v187, v187 op_sel_hi:[0,0,0] cbsz:2 blgp:2
	v_mfma_scale_f32_16x16x128_f8f6f4 v[108:111], v[194:199], v[32:37], v[108:111], v187, v187 op_sel_hi:[0,0,0] cbsz:2 blgp:2
	v_mfma_scale_f32_16x16x128_f8f6f4 v[104:107], v[200:205], v[32:37], v[104:107], v187, v187 op_sel_hi:[0,0,0] cbsz:2 blgp:2
	v_mfma_scale_f32_16x16x128_f8f6f4 v[96:99], v[206:211], v[32:37], v[96:99], v187, v187 op_sel_hi:[0,0,0] cbsz:2 blgp:2
	v_mfma_scale_f32_16x16x128_f8f6f4 v[80:83], v[46:51], v[40:45], v[80:83], v187, v187 op_sel_hi:[0,0,0] cbsz:2 blgp:2
	v_mfma_scale_f32_16x16x128_f8f6f4 v[72:75], v[194:199], v[40:45], v[72:75], v187, v187 op_sel_hi:[0,0,0] cbsz:2 blgp:2
	v_mfma_scale_f32_16x16x128_f8f6f4 v[64:67], v[200:205], v[40:45], v[64:67], v187, v187 op_sel_hi:[0,0,0] cbsz:2 blgp:2
	v_mfma_scale_f32_16x16x128_f8f6f4 v[56:59], v[206:211], v[40:45], v[56:59], v187, v187 op_sel_hi:[0,0,0] cbsz:2 blgp:2
	v_mfma_scale_f32_16x16x128_f8f6f4 v[52:55], v[46:51], v[188:193], v[52:55], v187, v187 op_sel_hi:[0,0,0] cbsz:2 blgp:2
	v_mfma_scale_f32_16x16x128_f8f6f4 v[48:51], v[194:199], v[188:193], v[224:227], v187, v187 op_sel_hi:[0,0,0] cbsz:2 blgp:2
	v_mfma_scale_f32_16x16x128_f8f6f4 v[44:47], v[200:205], v[188:193], v[212:215], v187, v187 op_sel_hi:[0,0,0] cbsz:2 blgp:2
	v_mfma_scale_f32_16x16x128_f8f6f4 v[40:43], v[206:211], v[188:193], v[216:219], v187, v187 op_sel_hi:[0,0,0] cbsz:2 blgp:2
.LBB1_6:
	s_add_i32 s2, s10, 0x100
	s_cmpk_gt_i32 s10, 0xb37
	s_cselect_b64 s[10:11], -1, 0
	s_and_b64 vcc, exec, s[10:11]
	s_mov_b32 s3, s13
	s_mov_b32 s35, s34
	s_cbranch_vccnz .LBB1_1
	s_ashr_i32 s3, s2, 31
	s_lshr_b32 s3, s3, 29
	s_add_i32 s3, s2, s3
	s_ashr_i32 s35, s3, 3
	s_and_b32 s3, s3, -8
	s_sub_i32 s3, s2, s3
	s_cmp_lt_i32 s3, 0
	s_cselect_b32 s36, s12, 0x187
	s_mul_i32 s3, s36, s3
	s_add_i32 s3, s3, s35
	s_ashr_i32 s35, s3, 31
	s_lshr_b32 s35, s35, 27
	s_add_i32 s35, s3, s35
	s_ashr_i32 s36, s35, 5
	s_lshl_b32 s38, s36, 2
	s_sub_i32 s36, 0x187, s38
	s_min_u32 s39, s36, 4
	s_andn2_b32 s35, s35, 31
	s_sub_i32 s3, s3, s35
	v_cvt_f32_ubyte0_e32 v3, s39
	v_cvt_f32_i32_e32 v2, s3
	v_rcp_iflag_f32_e32 v4, v3
	s_ashr_i32 s35, s3, 30
	s_or_b32 s35, s35, 1
	v_mul_f32_e32 v4, v2, v4
	v_trunc_f32_e32 v4, v4
	v_fma_f32 v2, -v4, v3, v2
	v_cvt_i32_f32_e32 v4, v4
	v_cmp_ge_f32_e64 s[36:37], |v2|, v3
	s_and_b64 s[36:37], s[36:37], exec
	s_cselect_b32 s35, s35, 0
	v_readfirstlane_b32 s36, v4
	s_add_i32 s36, s36, s35
	s_mul_i32 s35, s36, s39
	s_sub_i32 s3, s35, s3
	s_sext_i32_i8 s3, s3
	s_sub_i32 s3, s3, s38
	s_bfe_i64 s[38:39], s[36:37], 0x80000
	s_addk_i32 s3, 0x186
	s_mul_i32 s37, s38, 0x30000
	s_mul_hi_i32 s35, s38, 0x30000
	s_add_u32 s38, s6, s37
	s_addc_u32 s39, s7, s35
	s_mul_i32 s37, s3, 0x30000
	s_mul_hi_i32 s35, s3, 0x30000
	s_add_u32 s37, s4, s37
	s_addc_u32 s35, s5, s35
	s_add_u32 s42, s38, 0x2000
	s_addc_u32 s43, s39, 0
	s_add_u32 s44, s37, 0xfffff000
	s_addc_u32 s45, s35, -1
	s_and_b64 s[40:41], s[0:1], exec
	s_cselect_b32 s41, s43, s45
	s_cselect_b32 s40, s42, s44
	s_add_u32 s42, s37, 0x1000
	s_addc_u32 s43, s35, 0
	s_mov_b64 s[44:45], s[38:39]
	s_nop 0
	s_add_u32 s40, s38, 0x3000
	s_addc_u32 s41, s39, 0
	s_add_u32 s42, s38, 0x5000
	s_addc_u32 s43, s39, 0
	s_add_u32 s44, s37, 0x2000
	s_addc_u32 s45, s35, 0
	s_and_b64 s[38:39], s[0:1], exec
	s_cselect_b32 s39, s43, s45
	s_cselect_b32 s38, s42, s44
	s_add_u32 s42, s37, 0x4000
	s_addc_u32 s43, s35, 0
	s_sext_i32_i8 s35, s36
	s_nop 0
	s_mul_i32 s68, s35, 0x30000
	s_mul_hi_i32 s69, s35, 0x30000
	s_add_u32 s68, s6, s68
	s_addc_u32 s69, s7, s69
	s_mul_i32 s70, s3, 0x30000
	s_mul_hi_i32 s71, s3, 0x30000
	s_add_u32 s70, s4, s70
	s_addc_u32 s71, s5, s71
	s_mul_i32 s67, s66, 0x3000
	s_add_u32 s68, s68, s67
	s_addc_u32 s69, s69, 0
	s_add_u32 s70, s70, s67
	s_addc_u32 s71, s71, 0
	s_cmp_eq_u32 s74, 1
	s_cselect_b32 s68, s70, s68
	s_cselect_b32 s69, s71, s69
	s_add_u32 s68, s68, s75
	s_addc_u32 s69, s69, 0
	s_mov_b32 m0, s76
	s_nop 0
	global_load_lds_dwordx4 v228, s[68:69] offset:-3072
	global_load_lds_dwordx4 v228, s[68:69] offset:-2048
	global_load_lds_dwordx4 v228, s[68:69] offset:-1024
	global_load_lds_dwordx4 v228, s[68:69]
	global_load_lds_dwordx4 v228, s[68:69] offset:1024
	global_load_lds_dwordx4 v228, s[68:69] offset:2048
	s_branch .LBB1_1
